# baseline (speedup 1.0000x reference)
_Z16sum_layer_kernelPKfS0_Pf:
	s_load_dwordx4 s[4:7], s[0:1], 0x0
	s_load_dwordx2 s[8:9], s[0:1], 0x10
	v_lshrrev_b32_e32 v42, 6, v0
	v_bfe_u32 v41, v0, 5, 1
	v_and_b32_e32 v40, 31, v0
	v_readfirstlane_b32 s23, v42
	v_and_b32_e32 v43, 7, v0
	v_bfe_u32 v44, v0, 3, 3
	s_lshr_b32 s16, s23, 1
	s_and_b32 s17, s2, 0x1fe
	s_or_b32 s17, s17, s16
	s_and_b32 s16, s23, 1
	s_and_b32 s18, s2, 1
	s_lshl_b32 s18, s18, 1
	s_or_b32 s16, s16, s18
	s_lshl_b32 s3, s17, 12
	s_lshl_b32 s19, s17, 7
	s_lshl_b32 s16, s16, 21
	s_add_u32 s19, s19, s16
	s_lshl_b32 s23, s23, 12
	v_lshlrev_b32_e32 v1, 11, v41
	v_lshl_or_b32 v1, v40, 2, v1
	s_mov_b32 m0, s23
	v_lshrrev_b32_e32 v46, 1, v44
	v_xor_b32_e32 v46, v43, v46
	v_lshlrev_b32_e32 v46, 4, v46
	v_lshl_add_u32 v35, v44, 16, v46
	v_add_u32_e32 v35, s19, v35
	v_xor_b32_e32 v86, 64, v35
	s_mov_b32 s20, 0x7fc00
	s_mov_b32 s21, 0xff800
	s_mov_b32 s22, 0x17f400
	s_mov_b32 s14, 0x200000
	s_mov_b32 s15, 0x20000
	v_and_b32_e32 v45, 63, v0
	v_lshlrev_b32_e32 v37, 4, v45
	s_add_u32 s54, s23, 0x4000
	s_waitcnt lgkmcnt(0)
	s_mov_b32 s12, s6
	s_and_b32 s13, s7, 0xffff
	s_and_b32 s5, s5, 0xffff
	s_mov_b32 s6, 0x800000
	s_mov_b32 s7, s15
	s_mov_b32 m0, s54
	s_nop 0
	buffer_load_dwordx4 v37, s[12:15], s3 offen nt lds
	buffer_load_dwordx4 v37, s[12:15], s3 offen offset:1024 nt lds
	buffer_load_dwordx4 v37, s[12:15], s3 offen offset:2048 nt lds
	buffer_load_dwordx4 v37, s[12:15], s3 offen offset:3072 nt lds
	s_mov_b32 m0, s23
	s_nop 0
	buffer_load_dwordx4 v35, s[4:7], 0 offen nt lds
	buffer_load_dwordx4 v86, s[4:7], s20 offen offset:1024 nt lds
	buffer_load_dwordx4 v35, s[4:7], s21 offen offset:2048 nt lds
	buffer_load_dwordx4 v86, s[4:7], s22 offen offset:3072 nt lds
	v_and_b32_e32 v45, 63, v0
	v_lshlrev_b32_e32 v36, 2, v40
	v_lshl_add_u32 v36, v41, 18, v36
	v_add_u32_e32 v36, s19, v36
	v_bfe_u32 v47, v40, 1, 3
	v_lshlrev_b32_e32 v39, 2, v41
	v_xor_b32_e32 v39, v39, v47
	v_lshlrev_b32_e32 v39, 4, v39
	v_lshl_add_u32 v39, v40, 7, v39
	v_lshl_add_u32 v39, v42, 12, v39
	v_xor_b32_e32 v81, 16, v39
	v_xor_b32_e32 v82, 32, v39
	v_xor_b32_e32 v83, 48, v39
	v_cmp_gt_u32_e32 vcc, 32, v45
	v_mov_b32_e32 v34, 0xc1600000
	v_mov_b32_e32 v84, 0x3fb8aa3b
	v_mov_b32_e32 v85, 0x3f317218
	s_lshl_b32 s24, 1, 16
	s_lshl_b32 s25, 2, 16
	s_lshl_b32 s26, 3, 16
	s_lshl_b32 s27, 8, 16
	s_lshl_b32 s28, 9, 16
	s_lshl_b32 s29, 10, 16
	s_lshl_b32 s30, 11, 16
	s_lshl_b32 s31, 16, 16
	s_lshl_b32 s32, 17, 16
	s_lshl_b32 s33, 18, 16
	s_lshl_b32 s34, 19, 16
	s_lshl_b32 s35, 24, 16
	s_lshl_b32 s36, 25, 16
	s_lshl_b32 s37, 26, 16
	s_lshl_b32 s38, 27, 16
	s_and_b32 s9, s9, 0xffff
	s_mov_b32 s10, s6
	s_mov_b32 s11, s15
	v_lshl_add_u32 v38, v42, 12, v1
	v_add_u32_e32 v38, 0x4000, v38
	v_add_u32_e32 v87, 0x400, v38
	s_waitcnt vmcnt(4)
	ds_read2_b32 v[18:19], v38 offset0:0 offset1:32
	ds_read2_b32 v[20:21], v38 offset0:64 offset1:96
	ds_read2_b32 v[22:23], v38 offset0:128 offset1:160
	ds_read2_b32 v[24:25], v38 offset0:192 offset1:224
	ds_read2_b32 v[26:27], v87 offset0:0 offset1:32
	ds_read2_b32 v[28:29], v87 offset0:64 offset1:96
	ds_read2_b32 v[30:31], v87 offset0:128 offset1:160
	ds_read2_b32 v[32:33], v87 offset0:192 offset1:224
	s_waitcnt lgkmcnt(0)
	v_max3_f32 v48, v18, v19, v20
	v_max3_f32 v50, v21, v22, v23
	v_max3_f32 v48, v48, v24, v25
	v_max3_f32 v50, v50, v26, v27
	v_max3_f32 v48, v48, v28, v29
	v_max3_f32 v50, v50, v30, v31
	v_max3_f32 v48, v48, v32, v33
	v_max_f32_e32 v48, v48, v50
	v_mov_b32_e32 v50, v48
	s_nop 1
	v_permlane32_swap_b32_e32 v48, v50
	v_max_f32_e32 v48, v48, v50
	v_fmamk_f32 v48, v48, 0x3fb8aa3b, v34
	v_pk_fma_f32 v[18:19], v[18:19], v[84:85], v[48:49] op_sel_hi:[1,0,0] neg_lo:[0,0,1] neg_hi:[0,0,1]
	v_exp_f32_e32 v18, v18
	v_exp_f32_e32 v19, v19
	v_pk_fma_f32 v[20:21], v[20:21], v[84:85], v[48:49] op_sel_hi:[1,0,0] neg_lo:[0,0,1] neg_hi:[0,0,1]
	v_exp_f32_e32 v20, v20
	v_exp_f32_e32 v21, v21
	v_pk_fma_f32 v[22:23], v[22:23], v[84:85], v[48:49] op_sel_hi:[1,0,0] neg_lo:[0,0,1] neg_hi:[0,0,1]
	v_exp_f32_e32 v22, v22
	v_exp_f32_e32 v23, v23
	v_pk_fma_f32 v[24:25], v[24:25], v[84:85], v[48:49] op_sel_hi:[1,0,0] neg_lo:[0,0,1] neg_hi:[0,0,1]
	v_exp_f32_e32 v24, v24
	v_exp_f32_e32 v25, v25
	v_pk_fma_f32 v[26:27], v[26:27], v[84:85], v[48:49] op_sel_hi:[1,0,0] neg_lo:[0,0,1] neg_hi:[0,0,1]
	v_exp_f32_e32 v26, v26
	v_exp_f32_e32 v27, v27
	v_pk_fma_f32 v[28:29], v[28:29], v[84:85], v[48:49] op_sel_hi:[1,0,0] neg_lo:[0,0,1] neg_hi:[0,0,1]
	v_exp_f32_e32 v28, v28
	v_exp_f32_e32 v29, v29
	v_pk_fma_f32 v[30:31], v[30:31], v[84:85], v[48:49] op_sel_hi:[1,0,0] neg_lo:[0,0,1] neg_hi:[0,0,1]
	v_exp_f32_e32 v30, v30
	v_exp_f32_e32 v31, v31
	v_pk_fma_f32 v[32:33], v[32:33], v[84:85], v[48:49] op_sel_hi:[1,0,0] neg_lo:[0,0,1] neg_hi:[0,0,1]
	v_exp_f32_e32 v32, v32
	v_exp_f32_e32 v33, v33
	v_pk_add_f32 v[56:57], v[18:19], v[20:21]
	v_pk_add_f32 v[58:59], v[22:23], v[24:25]
	v_pk_add_f32 v[60:61], v[26:27], v[28:29]
	v_pk_add_f32 v[62:63], v[30:31], v[32:33]
	v_pk_add_f32 v[56:57], v[56:57], v[58:59]
	v_pk_add_f32 v[60:61], v[60:61], v[62:63]
	v_pk_add_f32 v[56:57], v[56:57], v[60:61]
	v_add_f32_e32 v50, v56, v57
	v_mov_b32_e32 v51, v50
	s_nop 1
	v_permlane32_swap_b32_e32 v50, v51
	v_add_f32_e32 v50, v50, v51
	v_log_f32_e32 v50, v50
	v_cvt_pk_f16_f32 v40, v18, v19
	v_cvt_pk_f16_f32 v41, v20, v21
	v_cvt_pk_f16_f32 v42, v22, v23
	v_cvt_pk_f16_f32 v43, v24, v25
	v_cvt_pk_f16_f32 v44, v26, v27
	v_cvt_pk_f16_f32 v45, v28, v29
	v_cvt_pk_f16_f32 v46, v30, v31
	v_cvt_pk_f16_f32 v47, v32, v33
	v_add_f32_e32 v50, 0x41600000, v50
	v_mul_f32_e32 v50, 0xbf317218, v50
	v_cndmask_b32_e64 v51, v50, 1.0, vcc
	s_waitcnt vmcnt(0)
	ds_read_b128 v[2:5], v39
	ds_read_b128 v[6:9], v81
	ds_read_b128 v[10:13], v82
	ds_read_b128 v[14:17], v83
	s_waitcnt lgkmcnt(2)
	v_max3_f32 v52, v2, v3, v4
	v_max3_f32 v53, v5, v6, v7
	v_max_f32_e32 v52, v52, v8
	v_max_f32_e32 v53, v53, v9
	s_waitcnt lgkmcnt(0)
	v_max3_f32 v52, v52, v10, v11
	v_max3_f32 v53, v53, v12, v13
	v_max3_f32 v52, v52, v14, v15
	v_max3_f32 v53, v53, v16, v17
	v_max_f32_e32 v52, v52, v53
	v_mov_b32_e32 v53, v52
	s_nop 1
	v_permlane32_swap_b32_e32 v52, v53
	v_max_f32_e32 v52, v52, v53
	v_cndmask_b32_e32 v54, 1.0, v52, vcc
	v_fmamk_f32 v48, v52, 0x3fb8aa3b, v34
	v_pk_fma_f32 v[2:3], v[2:3], v[84:85], v[48:49] op_sel_hi:[1,0,0] neg_lo:[0,0,1] neg_hi:[0,0,1]
	v_mfma_f32_32x32x2_f32 v[64:79], v54, v51, 0
	v_exp_f32_e32 v2, v2
	v_exp_f32_e32 v3, v3
	v_pk_fma_f32 v[4:5], v[4:5], v[84:85], v[48:49] op_sel_hi:[1,0,0] neg_lo:[0,0,1] neg_hi:[0,0,1]
	v_exp_f32_e32 v4, v4
	v_exp_f32_e32 v5, v5
	v_pk_fma_f32 v[6:7], v[6:7], v[84:85], v[48:49] op_sel_hi:[1,0,0] neg_lo:[0,0,1] neg_hi:[0,0,1]
	v_exp_f32_e32 v6, v6
	v_exp_f32_e32 v7, v7
	v_pk_fma_f32 v[8:9], v[8:9], v[84:85], v[48:49] op_sel_hi:[1,0,0] neg_lo:[0,0,1] neg_hi:[0,0,1]
	v_exp_f32_e32 v8, v8
	v_exp_f32_e32 v9, v9
	v_pk_fma_f32 v[10:11], v[10:11], v[84:85], v[48:49] op_sel_hi:[1,0,0] neg_lo:[0,0,1] neg_hi:[0,0,1]
	v_exp_f32_e32 v10, v10
	v_cvt_pk_f16_f32 v56, v2, v3
	v_cvt_pk_f16_f32 v57, v4, v5
	v_cvt_pk_f16_f32 v58, v6, v7
	v_cvt_pk_f16_f32 v59, v8, v9
	v_exp_f32_e32 v11, v11
	v_pk_fma_f32 v[12:13], v[12:13], v[84:85], v[48:49] op_sel_hi:[1,0,0] neg_lo:[0,0,1] neg_hi:[0,0,1]
	v_exp_f32_e32 v12, v12
	v_mfma_f32_32x32x16_f16 v[18:33], v[56:59], v[40:43], 0
	v_exp_f32_e32 v13, v13
	v_pk_fma_f32 v[14:15], v[14:15], v[84:85], v[48:49] op_sel_hi:[1,0,0] neg_lo:[0,0,1] neg_hi:[0,0,1]
	v_exp_f32_e32 v14, v14
	v_exp_f32_e32 v15, v15
	v_pk_fma_f32 v[16:17], v[16:17], v[84:85], v[48:49] op_sel_hi:[1,0,0] neg_lo:[0,0,1] neg_hi:[0,0,1]
	v_exp_f32_e32 v16, v16
	v_exp_f32_e32 v17, v17
	v_cvt_pk_f16_f32 v60, v10, v11
	v_cvt_pk_f16_f32 v61, v12, v13
	v_cvt_pk_f16_f32 v62, v14, v15
	v_cvt_pk_f16_f32 v63, v16, v17
	s_nop 1
	v_mfma_f32_32x32x16_f16 v[18:33], v[60:63], v[44:47], v[18:33]
	s_nop 11
	v_log_f32_e32 v18, v18
	v_log_f32_e32 v19, v19
	v_log_f32_e32 v20, v20
	v_log_f32_e32 v21, v21
	v_log_f32_e32 v22, v22
	v_log_f32_e32 v23, v23
	v_pk_fma_f32 v[64:65], v[18:19], v[84:85], v[64:65] op_sel:[0,1,0] op_sel_hi:[1,1,1]
	buffer_store_dword v64, v36, s[8:11], 0 offen
	buffer_store_dword v65, v36, s[8:11], s24 offen
	v_log_f32_e32 v24, v24
	v_log_f32_e32 v25, v25
	v_pk_fma_f32 v[66:67], v[20:21], v[84:85], v[66:67] op_sel:[0,1,0] op_sel_hi:[1,1,1]
	buffer_store_dword v66, v36, s[8:11], s25 offen
	buffer_store_dword v67, v36, s[8:11], s26 offen
	v_log_f32_e32 v26, v26
	v_log_f32_e32 v27, v27
	v_pk_fma_f32 v[68:69], v[22:23], v[84:85], v[68:69] op_sel:[0,1,0] op_sel_hi:[1,1,1]
	buffer_store_dword v68, v36, s[8:11], s27 offen
	buffer_store_dword v69, v36, s[8:11], s28 offen
	v_log_f32_e32 v28, v28
	v_log_f32_e32 v29, v29
	v_pk_fma_f32 v[70:71], v[24:25], v[84:85], v[70:71] op_sel:[0,1,0] op_sel_hi:[1,1,1]
	buffer_store_dword v70, v36, s[8:11], s29 offen
	buffer_store_dword v71, v36, s[8:11], s30 offen
	v_log_f32_e32 v30, v30
	v_log_f32_e32 v31, v31
	v_pk_fma_f32 v[72:73], v[26:27], v[84:85], v[72:73] op_sel:[0,1,0] op_sel_hi:[1,1,1]
	buffer_store_dword v72, v36, s[8:11], s31 offen
	buffer_store_dword v73, v36, s[8:11], s32 offen
	v_log_f32_e32 v32, v32
	v_log_f32_e32 v33, v33
	v_pk_fma_f32 v[74:75], v[28:29], v[84:85], v[74:75] op_sel:[0,1,0] op_sel_hi:[1,1,1]
	buffer_store_dword v74, v36, s[8:11], s33 offen
	buffer_store_dword v75, v36, s[8:11], s34 offen
	v_pk_fma_f32 v[76:77], v[30:31], v[84:85], v[76:77] op_sel:[0,1,0] op_sel_hi:[1,1,1]
	buffer_store_dword v76, v36, s[8:11], s35 offen
	buffer_store_dword v77, v36, s[8:11], s36 offen
	v_pk_fma_f32 v[78:79], v[32:33], v[84:85], v[78:79] op_sel:[0,1,0] op_sel_hi:[1,1,1]
	buffer_store_dword v78, v36, s[8:11], s37 offen
	buffer_store_dword v79, v36, s[8:11], s38 offen
	s_endpgm
